# final candidate + one static s_setprio 1 for waves 4-7 (younger half) during the attention phase
# baseline (speedup 1.0000x reference)
; __device__ __forceinline__ int lane_id_v() { int l; asm volatile("v_mbcnt_lo_u32_b32 %0, -1, 0\n\tv_mbcnt_hi_u32_b32 %0, -1, %0" : "=v"(l)); return l; }
; #define BAR_ALL() asm volatile("s_waitcnt lgkmcnt(0)\n\ts_barrier" ::: "memory")
; #define LOAD_ARGP() const CAS Args* argp = (const CAS Args*)__builtin_amdgcn_kernarg_segment_ptr(); asm volatile("" : "+s"(argp)); unsigned char* const ws = argp->ws; (void)ws
; #define LOK() (__builtin_amdgcn_readfirstlane((int)MISC[10]))
;     ...
;     if (ATT_SKEW && g == 1) BAR_ALL();
; __global__ void __launch_bounds__(512, 2) hymba_fwd(Args args) {
;     ...
;     if (PH(4)) {
;         const int lane = lane_id_v(), tid = wave * 64 + lane; (void)tid;
;         LOAD_ARGP();
;         const int r32 = lane & 31, hi = lane >> 5;
;         const float lam = MISCW[0];
;         const int lok = LOK();
.LBB0_591:
	s_cmp_ge_u32 s62, 4
	s_cbranch_scc0 .Lmy_prio_done
	s_setprio 1

; __device__ __forceinline__ int lane_id_v() { int l; asm volatile("v_mbcnt_lo_u32_b32 %0, -1, 0\n\tv_mbcnt_hi_u32_b32 %0, -1, %0" : "=v"(l)); return l; }
; __device__ __forceinline__ unsigned xb_ld(unsigned* p)              { return __hip_atomic_load(p, __ATOMIC_RELAXED, __HIP_MEMORY_SCOPE_AGENT); }
; __device__ __forceinline__ unsigned xb_add(unsigned* p, unsigned v) { return __hip_atomic_fetch_add(p, v, __ATOMIC_RELAXED, __HIP_MEMORY_SCOPE_AGENT); }
; #define XB_SPIN(cond, bar) do { unsigned _sp = 0; while (cond) { __builtin_amdgcn_s_sleep(1); \
;     if ((++_sp & 255u) == 0u) { if (xb_ld(&(bar)[XB_TMO])) break; if (_sp > XB_SPIN_CAP) { atomicAdd(&(bar)[XB_TMO], 1u); break; } } } } while (0)
; #define LOK() (__builtin_amdgcn_readfirstlane((int)MISC[10]))
; __device__ __forceinline__ void xcd_barrier_local(const XcdBarrier& b, int wave) {
;     asm volatile("s_waitcnt vmcnt(0)" ::: "memory");
;     __syncthreads();
;     if (wave == 0 && lane_id_v() == 0) {
;         unsigned* bar = b.bar;
;         __builtin_amdgcn_s_waitcnt(0);
;         const unsigned nloc = b.st[0] ? b.st[0] : 1u;
;         const unsigned old = xb_add(&bar[XB_LSUB(b.x)], 1u);
;         const unsigned gen = old / nloc;
;         if (old + 1u == (gen + 1u) * nloc) xb_add(&bar[XB_LGEN(b.x)], 1u);
;         else XB_SPIN(xb_ld(&bar[XB_LGEN(b.x)]) == gen, bar);
;         __builtin_amdgcn_fence(__ATOMIC_ACQUIRE, "agent");
;         asm volatile("s_waitcnt vmcnt(0)" ::: "memory");
;     }
; __global__ void __launch_bounds__(512, 2) hymba_fwd(Args args) {
;     ...
;     if (LOK()) xcd_barrier_local(bar, wave); else xcd_barrier(bar, wave);
.LBB0_681:
	s_setprio 0
	s_add_i32 s4, 0, 0x27e28
	v_mov_b32_e32 v0, s4
	ds_read_b32 v0, v0
	s_waitcnt lgkmcnt(0)
	v_readfirstlane_b32 s4, v0
	s_cmp_lg_u32 s4, 0
	s_cbranch_scc0 .LBB0_686
	s_waitcnt vmcnt(0)
	v_readlane_b32 s4, v248, 11
	v_readlane_b32 s5, v248, 12
	s_and_b64 vcc, exec, s[4:5]
	s_waitcnt vmcnt(0)
	s_barrier
	s_cbranch_vccnz .LBB0_706
	v_mbcnt_lo_u32_b32 v0, -1, 0
	v_mbcnt_hi_u32_b32 v0, -1, v0
	s_nop 0
	v_cmp_eq_u32_e32 vcc, 0, v0
	s_and_saveexec_b64 s[10:11], vcc
	s_cbranch_execz .LBB0_705
	s_add_i32 s4, 0, 0x27e20
	v_mov_b32_e32 v0, s4
	s_waitcnt vmcnt(0) expcnt(0) lgkmcnt(0)
	ds_read_b32 v0, v0
	s_waitcnt lgkmcnt(0)
	v_cmp_eq_u32_e32 vcc, 0, v0
	s_cbranch_vccnz .LBB0_687
	s_add_i32 s4, 0, 0x27e20
	v_mov_b32_e32 v0, s4
	ds_read_b32 v0, v0
	s_branch .LBB0_688
